# speedup vs baseline: 1.0256x; 1.0000x over previous
.LBB1_91:
	s_or_b64 exec, exec, s[40:41]
	v_mov_b32_e32 v7, 0
	s_waitcnt lgkmcnt(0)
	s_barrier
	ds_read_b32 v7, v7 offset:50176
	s_mov_b32 s7, 0
	s_waitcnt lgkmcnt(0)
	v_cmp_ne_u32_e32 vcc, 1, v7
	s_cbranch_vccnz .LBB1_95
	s_lshl_b64 s[38:39], s[6:7], 7
	s_lshl_b64 s[6:7], s[6:7], 10
	s_add_u32 s23, s18, s6
	s_addc_u32 s40, s19, s7
	s_lshl_b64 s[6:7], s[30:31], 3
	s_add_u32 s6, s23, s6
	s_addc_u32 s7, s40, s7
	global_load_dwordx2 v[6:7], v6, s[6:7] sc1
	s_add_u32 s42, s38, s30
	s_addc_u32 s43, s39, 0
	s_lshl_b64 s[42:43], s[42:43], 7
	s_add_u32 s42, s16, s42
	s_addc_u32 s43, s17, s43
	v_add_lshl_u32 v54, v13, v11, 3
	v_add_lshl_u32 v55, v13, v9, 3
	s_nop 4
	global_load_dwordx2 v[24:25], v54, s[42:43] sc1
	global_load_dwordx2 v[26:27], v54, s[42:43] offset:8 sc1
	global_load_dwordx2 v[42:43], v55, s[42:43] sc1
	global_load_dwordx2 v[44:45], v55, s[42:43] offset:8 sc1
	v_add_lshl_u32 v54, v13, v5, 3
	v_add_lshl_u32 v55, v13, v3, 3
	global_load_dwordx2 v[46:47], v54, s[42:43] sc1
	global_load_dwordx2 v[48:49], v54, s[42:43] offset:8 sc1
	global_load_dwordx2 v[50:51], v55, s[42:43] sc1
	global_load_dwordx2 v[52:53], v55, s[42:43] offset:8 sc1
	s_and_saveexec_b64 s[6:7], s[4:5]
	s_cbranch_execz .LBB1_94
	v_max_f32_e32 v14, v206, v206
	s_waitcnt vmcnt(8)
	v_max_f32_e32 v15, v6, v6
	v_max_f32_e32 v14, v14, v15
	v_sub_f32_e32 v6, v6, v14
	v_sub_f32_e32 v15, v206, v14
	v_exp_f32_e32 v6, v6
	v_exp_f32_e32 v14, v15
	v_mul_f32_e32 v6, v6, v7
	v_fma_f32 v7, v207, v14, v6
	v_div_scale_f32 v15, s[4:5], v7, v7, 1.0
	v_rcp_f32_e32 v20, v15
	v_mul_f32_e32 v14, v207, v14
	v_fma_f32 v21, -v15, v20, 1.0
	v_fmac_f32_e32 v20, v21, v20
	v_div_scale_f32 v21, vcc, 1.0, v7, 1.0
	v_mul_f32_e32 v22, v21, v20
	v_fma_f32 v23, -v15, v22, v21
	v_fmac_f32_e32 v22, v23, v20
	v_fma_f32 v15, -v15, v22, v21
	v_div_fmas_f32 v15, v15, v20, v22
	v_div_fixup_f32 v7, v15, v7, 1.0
	v_lshl_add_u32 v15, v199, 2, s64
	v_mul_f32_e32 v14, v14, v7
	v_mul_f32_e32 v6, v6, v7
	v_add_u32_e32 v7, 0xc000, v15
	ds_write2_b32 v7, v14, v6 offset1:32
.LBB1_94:
	s_or_b64 exec, exec, s[6:7]
	s_lshl_b32 s4, s28, 1
	s_add_u32 s6, s14, s4
	s_addc_u32 s7, s15, 0
	s_lshl_b64 s[4:5], s[36:37], 1
	s_add_u32 s4, s6, s4
	s_addc_u32 s5, s7, s5
	s_add_u32 s6, s38, s30
	s_addc_u32 s7, s39, 0
	s_lshl_b64 s[6:7], s[6:7], 7
	s_add_u32 s6, s16, s6
	s_addc_u32 s7, s17, s7
	s_waitcnt vmcnt(8)
	v_lshlrev_b32_e32 v6, 3, v13
	v_mov_b32_e32 v7, 0
	v_lshl_add_u64 v[14:15], s[6:7], 0, v[6:7]
	v_lshlrev_b32_e32 v6, 3, v11
	s_waitcnt lgkmcnt(0)
	v_lshl_add_u64 v[20:21], v[14:15], 0, v[6:7]
	s_nop 0
	s_nop 0
	s_nop 0
	s_nop 0
	s_nop 0
	s_nop 0
	v_lshl_add_u32 v6, v1, 2, s64
	ds_read_b128 v[20:23], v19
	v_add_u32_e32 v40, 0xc000, v6
	ds_read2_b32 v[28:29], v40 offset1:32
	v_lshlrev_b32_e32 v6, 3, v9
	v_lshl_add_u64 v[30:31], v[14:15], 0, v[6:7]
	s_waitcnt lgkmcnt(1)
	v_cvt_f32_f16_e32 v32, v20
	v_cvt_f32_f16_sdwa v33, v20 dst_sel:DWORD dst_unused:UNUSED_PAD src0_sel:WORD_1
	v_cvt_f32_f16_e32 v20, v21
	v_cvt_f32_f16_sdwa v21, v21 dst_sel:DWORD dst_unused:UNUSED_PAD src0_sel:WORD_1
	v_cvt_f32_f16_e32 v34, v22
	v_cvt_f32_f16_sdwa v35, v22 dst_sel:DWORD dst_unused:UNUSED_PAD src0_sel:WORD_1
	v_cvt_f32_f16_e32 v22, v23
	v_cvt_f32_f16_sdwa v23, v23 dst_sel:DWORD dst_unused:UNUSED_PAD src0_sel:WORD_1
	s_waitcnt lgkmcnt(0)
	v_mov_b32_e32 v6, v29
	v_mov_b32_e32 v11, v7
	v_mov_b32_e32 v13, v7
	v_lshl_add_u64 v[10:11], s[4:5], 0, v[10:11]
	v_lshl_add_u64 v[12:13], v[10:11], 0, v[12:13]
	v_mov_b32_e32 v9, v7
	v_lshl_add_u64 v[8:9], v[10:11], 0, v[8:9]
	s_waitcnt vmcnt(7)
	v_cvt_f32_f16_e32 v36, v24
	v_cvt_f32_f16_sdwa v37, v24 dst_sel:DWORD dst_unused:UNUSED_PAD src0_sel:WORD_1
	v_cvt_f32_f16_e32 v24, v25
	v_cvt_f32_f16_sdwa v25, v25 dst_sel:DWORD dst_unused:UNUSED_PAD src0_sel:WORD_1
	s_waitcnt vmcnt(6)
	v_cvt_f32_f16_e32 v38, v26
	v_cvt_f32_f16_sdwa v39, v26 dst_sel:DWORD dst_unused:UNUSED_PAD src0_sel:WORD_1
	v_cvt_f32_f16_e32 v26, v27
	v_cvt_f32_f16_sdwa v27, v27 dst_sel:DWORD dst_unused:UNUSED_PAD src0_sel:WORD_1
	v_pk_mul_f32 v[36:37], v[6:7], v[36:37] op_sel_hi:[0,1]
	v_pk_mul_f32 v[24:25], v[6:7], v[24:25] op_sel_hi:[0,1]
	v_pk_mul_f32 v[38:39], v[6:7], v[38:39] op_sel_hi:[0,1]
	v_pk_mul_f32 v[26:27], v[6:7], v[26:27] op_sel_hi:[0,1]
	v_pk_fma_f32 v[32:33], v[28:29], v[32:33], v[36:37] op_sel_hi:[0,1,1]
	v_pk_fma_f32 v[24:25], v[28:29], v[20:21], v[24:25] op_sel_hi:[0,1,1]
	v_pk_fma_f32 v[34:35], v[28:29], v[34:35], v[38:39] op_sel_hi:[0,1,1]
	v_pk_fma_f32 v[26:27], v[28:29], v[22:23], v[26:27] op_sel_hi:[0,1,1]
	v_cvt_pk_f16_f32 v20, v32, v33
	v_cvt_pk_f16_f32 v21, v24, v25
	v_cvt_pk_f16_f32 v22, v34, v35
	v_cvt_pk_f16_f32 v23, v26, v27
	global_store_dwordx4 v[12:13], v[20:23], off sc1
	s_waitcnt vmcnt(5)
	v_mov_b32_e32 v12, v42
	v_mov_b32_e32 v13, v43
	v_mov_b32_e32 v22, v44
	v_mov_b32_e32 v23, v45
	ds_read_b128 v[18:21], v18
	ds_read2_b32 v[24:25], v40 offset0:8 offset1:40
	v_lshlrev_b32_e32 v6, 3, v5
	v_lshl_add_u64 v[26:27], v[14:15], 0, v[6:7]
	v_mov_b32_e32 v5, v7
	s_waitcnt lgkmcnt(1)
	v_cvt_f32_f16_e32 v28, v18
	v_cvt_f32_f16_sdwa v29, v18 dst_sel:DWORD dst_unused:UNUSED_PAD src0_sel:WORD_1
	v_cvt_f32_f16_e32 v18, v19
	v_cvt_f32_f16_sdwa v19, v19 dst_sel:DWORD dst_unused:UNUSED_PAD src0_sel:WORD_1
	v_cvt_f32_f16_e32 v30, v20
	v_cvt_f32_f16_sdwa v31, v20 dst_sel:DWORD dst_unused:UNUSED_PAD src0_sel:WORD_1
	v_cvt_f32_f16_e32 v20, v21
	v_cvt_f32_f16_sdwa v21, v21 dst_sel:DWORD dst_unused:UNUSED_PAD src0_sel:WORD_1
	s_waitcnt lgkmcnt(0)
	v_mov_b32_e32 v6, v25
	v_lshl_add_u64 v[4:5], v[10:11], 0, v[4:5]
	s_waitcnt vmcnt(5)
	v_cvt_f32_f16_e32 v32, v12
	v_cvt_f32_f16_sdwa v33, v12 dst_sel:DWORD dst_unused:UNUSED_PAD src0_sel:WORD_1
	v_cvt_f32_f16_e32 v12, v13
	v_cvt_f32_f16_sdwa v13, v13 dst_sel:DWORD dst_unused:UNUSED_PAD src0_sel:WORD_1
	s_waitcnt vmcnt(5)
	v_cvt_f32_f16_e32 v34, v22
	v_cvt_f32_f16_sdwa v35, v22 dst_sel:DWORD dst_unused:UNUSED_PAD src0_sel:WORD_1
	v_cvt_f32_f16_e32 v22, v23
	v_cvt_f32_f16_sdwa v23, v23 dst_sel:DWORD dst_unused:UNUSED_PAD src0_sel:WORD_1
	v_pk_mul_f32 v[32:33], v[6:7], v[32:33] op_sel_hi:[0,1]
	v_pk_mul_f32 v[12:13], v[6:7], v[12:13] op_sel_hi:[0,1]
	v_pk_mul_f32 v[34:35], v[6:7], v[34:35] op_sel_hi:[0,1]
	v_pk_mul_f32 v[22:23], v[6:7], v[22:23] op_sel_hi:[0,1]
	v_pk_fma_f32 v[28:29], v[24:25], v[28:29], v[32:33] op_sel_hi:[0,1,1]
	v_pk_fma_f32 v[12:13], v[24:25], v[18:19], v[12:13] op_sel_hi:[0,1,1]
	v_pk_fma_f32 v[30:31], v[24:25], v[30:31], v[34:35] op_sel_hi:[0,1,1]
	v_pk_fma_f32 v[22:23], v[24:25], v[20:21], v[22:23] op_sel_hi:[0,1,1]
	v_cvt_pk_f16_f32 v18, v28, v29
	v_cvt_pk_f16_f32 v19, v12, v13
	v_cvt_pk_f16_f32 v20, v30, v31
	v_cvt_pk_f16_f32 v21, v22, v23
	global_store_dwordx4 v[8:9], v[18:21], off sc1
	s_waitcnt vmcnt(4)
	v_mov_b32_e32 v8, v46
	v_mov_b32_e32 v9, v47
	v_mov_b32_e32 v12, v48
	v_mov_b32_e32 v13, v49
	ds_read_b128 v[18:21], v17
	ds_read2_b32 v[22:23], v40 offset0:16 offset1:48
	v_lshlrev_b32_e32 v6, 3, v3
	v_lshl_add_u64 v[24:25], v[14:15], 0, v[6:7]
	v_mov_b32_e32 v3, v7
	s_waitcnt lgkmcnt(1)
	v_cvt_f32_f16_e32 v14, v18
	v_cvt_f32_f16_sdwa v15, v18 dst_sel:DWORD dst_unused:UNUSED_PAD src0_sel:WORD_1
	v_cvt_f32_f16_e32 v18, v19
	v_cvt_f32_f16_sdwa v19, v19 dst_sel:DWORD dst_unused:UNUSED_PAD src0_sel:WORD_1
	v_cvt_f32_f16_e32 v26, v20
	v_cvt_f32_f16_sdwa v27, v20 dst_sel:DWORD dst_unused:UNUSED_PAD src0_sel:WORD_1
	v_cvt_f32_f16_e32 v20, v21
	v_cvt_f32_f16_sdwa v21, v21 dst_sel:DWORD dst_unused:UNUSED_PAD src0_sel:WORD_1
	s_waitcnt lgkmcnt(0)
	v_mov_b32_e32 v6, v23
	v_lshl_add_u64 v[2:3], v[10:11], 0, v[2:3]
	s_waitcnt vmcnt(4)
	v_cvt_f32_f16_e32 v28, v8
	v_cvt_f32_f16_sdwa v29, v8 dst_sel:DWORD dst_unused:UNUSED_PAD src0_sel:WORD_1
	v_cvt_f32_f16_e32 v8, v9
	v_cvt_f32_f16_sdwa v9, v9 dst_sel:DWORD dst_unused:UNUSED_PAD src0_sel:WORD_1
	s_waitcnt vmcnt(4)
	v_cvt_f32_f16_e32 v30, v12
	v_cvt_f32_f16_sdwa v31, v12 dst_sel:DWORD dst_unused:UNUSED_PAD src0_sel:WORD_1
	v_cvt_f32_f16_e32 v12, v13
	v_cvt_f32_f16_sdwa v13, v13 dst_sel:DWORD dst_unused:UNUSED_PAD src0_sel:WORD_1
	v_pk_mul_f32 v[28:29], v[6:7], v[28:29] op_sel_hi:[0,1]
	v_pk_mul_f32 v[8:9], v[6:7], v[8:9] op_sel_hi:[0,1]
	v_pk_mul_f32 v[30:31], v[6:7], v[30:31] op_sel_hi:[0,1]
	v_pk_mul_f32 v[12:13], v[6:7], v[12:13] op_sel_hi:[0,1]
	v_pk_fma_f32 v[14:15], v[22:23], v[14:15], v[28:29] op_sel_hi:[0,1,1]
	v_pk_fma_f32 v[8:9], v[22:23], v[18:19], v[8:9] op_sel_hi:[0,1,1]
	v_pk_fma_f32 v[18:19], v[22:23], v[26:27], v[30:31] op_sel_hi:[0,1,1]
	v_pk_fma_f32 v[20:21], v[22:23], v[20:21], v[12:13] op_sel_hi:[0,1,1]
	v_cvt_pk_f16_f32 v12, v14, v15
	v_cvt_pk_f16_f32 v13, v8, v9
	v_cvt_pk_f16_f32 v14, v18, v19
	v_cvt_pk_f16_f32 v15, v20, v21
	global_store_dwordx4 v[4:5], v[12:15], off sc1
	s_waitcnt vmcnt(3)
	v_mov_b32_e32 v4, v50
	v_mov_b32_e32 v5, v51
	v_mov_b32_e32 v8, v52
	v_mov_b32_e32 v9, v53
	ds_read_b128 v[12:15], v16
	ds_read2_b32 v[16:17], v40 offset0:24 offset1:56
	s_waitcnt lgkmcnt(1)
	v_cvt_f32_f16_e32 v6, v12
	v_cvt_f32_f16_sdwa v7, v12 dst_sel:DWORD dst_unused:UNUSED_PAD src0_sel:WORD_1
	v_cvt_f32_f16_e32 v18, v13
	v_cvt_f32_f16_sdwa v19, v13 dst_sel:DWORD dst_unused:UNUSED_PAD src0_sel:WORD_1
	v_cvt_f32_f16_e32 v20, v14
	v_cvt_f32_f16_sdwa v21, v14 dst_sel:DWORD dst_unused:UNUSED_PAD src0_sel:WORD_1
	v_cvt_f32_f16_e32 v14, v15
	v_cvt_f32_f16_sdwa v15, v15 dst_sel:DWORD dst_unused:UNUSED_PAD src0_sel:WORD_1
	s_waitcnt lgkmcnt(0)
	v_mov_b32_e32 v12, v17
	s_waitcnt vmcnt(3)
	v_cvt_f32_f16_e32 v22, v4
	v_cvt_f32_f16_sdwa v23, v4 dst_sel:DWORD dst_unused:UNUSED_PAD src0_sel:WORD_1
	v_cvt_f32_f16_e32 v4, v5
	v_cvt_f32_f16_sdwa v5, v5 dst_sel:DWORD dst_unused:UNUSED_PAD src0_sel:WORD_1
	s_waitcnt vmcnt(3)
	v_cvt_f32_f16_e32 v24, v8
	v_cvt_f32_f16_sdwa v25, v8 dst_sel:DWORD dst_unused:UNUSED_PAD src0_sel:WORD_1
	v_cvt_f32_f16_e32 v8, v9
	v_cvt_f32_f16_sdwa v9, v9 dst_sel:DWORD dst_unused:UNUSED_PAD src0_sel:WORD_1
	v_pk_mul_f32 v[22:23], v[12:13], v[22:23] op_sel_hi:[0,1]
	v_pk_mul_f32 v[4:5], v[12:13], v[4:5] op_sel_hi:[0,1]
	v_pk_mul_f32 v[24:25], v[12:13], v[24:25] op_sel_hi:[0,1]
	v_pk_mul_f32 v[8:9], v[12:13], v[8:9] op_sel_hi:[0,1]
	v_pk_fma_f32 v[6:7], v[16:17], v[6:7], v[22:23] op_sel_hi:[0,1,1]
	v_pk_fma_f32 v[12:13], v[16:17], v[18:19], v[4:5] op_sel_hi:[0,1,1]
	v_pk_fma_f32 v[18:19], v[16:17], v[20:21], v[24:25] op_sel_hi:[0,1,1]
	v_pk_fma_f32 v[8:9], v[16:17], v[14:15], v[8:9] op_sel_hi:[0,1,1]
	v_cvt_pk_f16_f32 v4, v6, v7
	v_cvt_pk_f16_f32 v5, v12, v13
	v_cvt_pk_f16_f32 v6, v18, v19
	v_cvt_pk_f16_f32 v7, v8, v9
	global_store_dwordx4 v[2:3], v[4:7], off sc1
